# v032
# speedup vs baseline: 1.0752x; 1.0201x over previous
.Ltok_done:
	v_cmp_ne_u32_e32 vcc, 0, v7
	s_and_saveexec_b64 s[6:7], vcc
	v_mov_b32_e32 v1, 1
	v_mov_b32_e32 v2, 0
	ds_write_b32 v2, v1 offset:24832
	s_or_b64 exec, exec, s[6:7]
	s_mov_b32 s5, 0
	s_cmp_eq_u32 s16, 0
	s_cselect_b64 vcc, -1, 0
	v_mov_b32_e32 v157, 0
	s_waitcnt lgkmcnt(0)
	s_barrier
	ds_read_b32 v1, v157 offset:24832
	v_lshrrev_b32_e32 v108, 6, v0
	v_and_b32_e32 v4, 63, v0
	s_movk_i32 s0, 0x1000
	v_mov_b32_e32 v9, v157
	s_waitcnt lgkmcnt(0)
	v_readfirstlane_b32 s4, v1
	v_lshl_or_b32 v1, s16, 3, v108
	v_mul_u32_u24_e32 v1, 0x300, v1
	v_lshlrev_b32_e32 v156, 4, v1
	v_lshl_add_u64 v[2:3], s[8:9], 0, v[156:157]
	v_lshlrev_b32_e32 v156, 4, v4
	v_lshl_add_u64 v[2:3], v[2:3], 0, v[156:157]
	v_add_co_u32_e64 v4, s[0:1], s0, v2
	v_lshl_or_b32 v1, s16, 4, v108
	s_nop 0
	v_addc_co_u32_e64 v5, s[0:1], 0, v3, s[0:1]
	s_movk_i32 s0, 0x2000
	s_nop 0
	v_add_co_u32_e64 v6, s[0:1], s0, v2
	v_or_b32_e32 v8, 8, v1
	s_nop 0
	v_addc_co_u32_e64 v7, s[0:1], 0, v3, s[0:1]
	s_add_u32 s0, s8, 0x30000
	v_mul_u32_u24_e32 v8, 0xc0, v8
	s_addc_u32 s1, s9, 0
	v_lshlrev_b32_e32 v8, 4, v8
	v_mul_u32_u24_e32 v1, 0xc0, v1
	v_lshl_add_u64 v[92:93], s[0:1], 0, v[8:9]
	v_lshlrev_b32_e32 v8, 4, v1
	s_cmp_lg_u32 s4, 0
	v_lshl_add_u64 v[8:9], s[0:1], 0, v[8:9]
	s_cselect_b64 s[12:13], -1, 0
	s_lshl_b32 s0, s16, 11
	s_add_u32 s0, s8, s0
	s_addc_u32 s1, s9, 0
	v_and_b32_e32 v10, 0x1c0, v0
	v_mov_b32_e32 v11, v157
	v_lshl_add_u64 v[10:11], s[0:1], 0, v[10:11]
	v_and_b32_e32 v12, 48, v0
	v_mov_b32_e32 v13, v157
	v_and_b32_e32 v161, 15, v0
	v_lshl_add_u64 v[10:11], v[10:11], 0, v[12:13]
	s_mov_b64 s[0:1], 0x48000
	v_lshrrev_b32_e32 v12, 5, v0
	v_bfe_u32 v13, v0, 5, 1
	v_bfe_u32 v109, v0, 4, 2
	v_lshl_add_u64 v[72:73], v[10:11], 0, s[0:1]
	s_mov_b32 s0, 0x48000
	v_lshlrev_b32_e32 v1, 3, v0
	v_and_or_b32 v12, v12, 2, v13
	v_lshlrev_b32_e32 v13, 4, v161
	v_lshrrev_b32_e32 v0, 1, v0
	v_add_co_u32_e64 v10, s[0:1], s0, v10
	v_and_b32_e32 v1, 0xc00, v1
	v_lshl_or_b32 v12, v12, 8, v13
	v_and_b32_e32 v0, 8, v0
	v_lshl_add_u64 v[8:9], v[8:9], 0, v[156:157]
	v_addc_co_u32_e64 v11, s[0:1], 0, v11, s[0:1]
	v_or3_b32 v163, v12, v1, v0
	global_load_dwordx4 v[12:15], v[2:3], off
	global_load_dwordx4 v[16:19], v[2:3], off offset:1024
	global_load_dwordx4 v[20:23], v[2:3], off offset:2048
	global_load_dwordx4 v[24:27], v[2:3], off offset:3072
	global_load_dwordx4 v[28:31], v[6:7], off offset:-4096
	global_load_dwordx4 v[32:35], v[6:7], off
	global_load_dwordx4 v[36:39], v[6:7], off offset:1024
	global_load_dwordx4 v[40:43], v[6:7], off offset:2048
	global_load_dwordx4 v[44:47], v[6:7], off offset:3072
	global_load_dwordx4 v[48:51], v[4:5], off offset:1024
	global_load_dwordx4 v[52:55], v[4:5], off offset:2048
	global_load_dwordx4 v[56:59], v[4:5], off offset:3072
	global_load_dwordx4 v[60:63], v[8:9], off
	global_load_dwordx4 v[64:67], v[8:9], off offset:1024
	global_load_dwordx4 v[68:71], v[8:9], off offset:2048
	global_load_dwordx4 v[76:79], v[72:73], off offset:512
	global_load_dwordx4 v[80:83], v[72:73], off offset:1024
	global_load_dwordx4 v[84:87], v[10:11], off
	global_load_dwordx4 v[88:91], v[72:73], off offset:1536
	s_and_b64 s[0:1], vcc, exec
	s_cselect_b32 s14, 0, 0x7f
	s_lshl_b32 s7, s16, 22
	s_add_u32 s0, s8, s7
	s_addc_u32 s1, s9, 0
	v_lshlrev_b32_e32 v94, 12, v108
	v_mov_b32_e32 v95, v157
	v_lshl_add_u64 v[0:1], s[0:1], 0, v[94:95]
	v_lshl_add_u64 v[0:1], v[0:1], 0, v[156:157]
	s_mov_b64 s[0:1], 0xc9000
	v_lshl_add_u64 v[158:159], v[0:1], 0, s[0:1]
	s_lshl_b32 s4, s14, 15
	v_lshl_add_u64 v[96:97], v[158:159], 0, s[4:5]
	global_load_dwordx4 v[72:75], v[96:97], off
	global_load_dwordx4 v[8:11], v[96:97], off offset:1024
	global_load_dwordx4 v[4:7], v[96:97], off offset:2048
	global_load_dwordx4 v[0:3], v[96:97], off offset:3072
	v_mul_u32_u24_e32 v95, 0x104, v161
	ds_read_b32 v96, v95 offset:16512
	ds_read_b32 v95, v95 offset:20672
	s_movk_i32 s6, 0x410
	s_movk_i32 s0, 0x104
	v_mov_b32_e32 v97, 0x4080
	s_waitcnt lgkmcnt(1)
	v_lshrrev_b32_e32 v178, 16, v96
	v_and_b32_e32 v96, 0xffff, v96
	v_mad_u32_u24 v176, v161, s0, v97
	v_mad_u32_u24 v110, v109, s6, v96
	s_waitcnt lgkmcnt(0)
	v_lshrrev_b32_e32 v177, 16, v95
	v_and_b32_e32 v95, 0xffff, v95
	s_and_b64 s[0:1], vcc, exec
	v_mad_u32_u24 v111, v109, s6, v95
	s_cselect_b32 s15, 1, -1
	s_or_b32 s0, s7, s4
	ds_read_b128 v[120:123], v110 offset:8192
	ds_read_b128 v[116:119], v111 offset:8192
	v_lshl_add_u64 v[164:165], v[92:93], 0, v[156:157]
	v_or3_b32 v92, s0, v94, v156
	v_mov_b32_e32 v93, v157
	v_lshl_add_u64 v[92:93], s[8:9], 0, v[92:93]
	s_mov_b64 s[0:1], 0xc9800
	s_lshl_b32 s4, s15, 1
	v_mov_b32_e32 v106, v157
	v_mov_b32_e32 v107, v157
	v_lshl_add_u64 v[166:167], v[92:93], 0, s[0:1]
	s_ashr_i32 s5, s4, 31
	v_mov_b32_e32 v100, 0xc47a0000
	v_mov_b32_e32 v104, v157
	v_mov_b32_e32 v105, v157
	v_cndmask_b32_e64 v92, 0, 1, s[12:13]
	v_mov_b64_e32 v[142:143], v[106:107]
	s_lshl_b64 s[6:7], s[4:5], 15
	s_add_i32 s8, s14, s15
	v_mov_b32_e32 v101, v100
	v_mov_b32_e32 v102, v100
	v_mov_b32_e32 v103, v100
	s_mov_b32 s5, -2
	v_cmp_ne_u32_e64 s[0:1], 1, v92
	v_mov_b32_e32 v172, v157
	v_mov_b32_e32 v173, v157
	v_mov_b32_e32 v174, v157
	v_mov_b32_e32 v175, v157
	v_mov_b32_e32 v96, v157
	v_mov_b32_e32 v97, v157
	v_mov_b32_e32 v98, v157
	v_mov_b32_e32 v99, v157
	v_mov_b32_e32 v92, v157
	v_mov_b32_e32 v93, v157
	v_mov_b32_e32 v94, v157
	v_mov_b32_e32 v95, v157
	v_mov_b32_e32 v144, v157
	v_mov_b32_e32 v145, v157
	v_mov_b32_e32 v146, v157
	v_mov_b32_e32 v147, v157
	v_mov_b32_e32 v132, v157
	v_mov_b32_e32 v133, v157
	v_mov_b32_e32 v134, v157
	v_mov_b32_e32 v135, v157
	v_mov_b32_e32 v128, v157
	v_mov_b32_e32 v129, v157
	v_mov_b32_e32 v130, v157
	v_mov_b32_e32 v131, v157
	v_mov_b32_e32 v136, v157
	v_mov_b32_e32 v137, v157
	v_mov_b32_e32 v138, v157
	v_mov_b32_e32 v139, v157
	v_mov_b32_e32 v124, v157
	v_mov_b32_e32 v125, v157
	v_mov_b32_e32 v126, v157
	v_mov_b32_e32 v127, v157
	v_mov_b32_e32 v170, v157
	v_mov_b32_e32 v171, v157
	v_mov_b32_e32 v168, v157
	v_mov_b32_e32 v169, v157
	v_lshlrev_b32_e32 v162, 4, v108
	v_mul_u32_u24_e32 v157, 0x410, v109
	v_lshlrev_b32_e32 v160, 2, v109
	v_mov_b64_e32 v[140:141], v[104:105]
	v_mov_b32_e32 v144, 0
	v_mov_b32_e32 v145, 0
	v_mov_b32_e32 v146, 0
	v_mov_b32_e32 v147, 0
	v_mov_b32_e32 v148, 0xc47a0000
	v_mov_b32_e32 v149, 0xc47a0000
	v_mov_b32_e32 v150, 0xc47a0000
	v_mov_b32_e32 v151, 0xc47a0000
	v_mov_b32_e32 v152, 0
	v_mov_b32_e32 v153, 0
	v_mov_b32_e32 v154, 0
	v_mov_b32_e32 v155, 0
	s_movk_i32 s17, 0x61
	global_load_dwordx4 v[206:209], v[164:165], off
	global_load_dwordx4 v[210:213], v[164:165], off offset:1024
	global_load_dwordx4 v[214:217], v[164:165], off offset:2048
	v_add_u32_e32 v252, v162, v160
	v_mul_u32_u24_e32 v252, 12, v252
	v_lshl_add_u32 v229, v161, 4, v157
	v_mul_u32_u24_e32 v230, 0x610, v161
	v_add_u32_e32 v230, v230, v252
	v_add_u32_e32 v231, 0x18400, v252
	s_waitcnt vmcnt(0) lgkmcnt(0)
	ds_read_b128 v[190:193], v229 offset:8192
	s_waitcnt lgkmcnt(0)
	v_mfma_f32_16x16x32_f16 v[194:197], v[60:63], v[190:193], v[84:87]
	v_mfma_f32_16x16x32_f16 v[198:201], v[64:67], v[190:193], v[76:79]
	v_mfma_f32_16x16x32_f16 v[202:205], v[68:71], v[190:193], v[88:91]
	s_nop 7
	s_nop 1
	ds_write_b128 v230, v[194:197] offset:24848
	ds_write_b128 v230, v[198:201] offset:24864
	ds_write_b128 v230, v[202:205] offset:24880
	v_add_u32_e32 v230, 0x6100, v230
	ds_read_b128 v[190:193], v229 offset:8448
	s_waitcnt lgkmcnt(0)
	v_mfma_f32_16x16x32_f16 v[194:197], v[60:63], v[190:193], v[84:87]
	v_mfma_f32_16x16x32_f16 v[198:201], v[64:67], v[190:193], v[76:79]
	v_mfma_f32_16x16x32_f16 v[202:205], v[68:71], v[190:193], v[88:91]
	s_nop 7
	s_nop 1
	ds_write_b128 v230, v[194:197] offset:24848
	ds_write_b128 v230, v[198:201] offset:24864
	ds_write_b128 v230, v[202:205] offset:24880
	v_add_u32_e32 v230, 0x6100, v230
	ds_read_b128 v[190:193], v229 offset:12864
	s_waitcnt lgkmcnt(0)
	v_mfma_f32_16x16x32_f16 v[194:197], v[206:209], v[190:193], v[84:87]
	v_mfma_f32_16x16x32_f16 v[198:201], v[210:213], v[190:193], v[76:79]
	v_mfma_f32_16x16x32_f16 v[202:205], v[214:217], v[190:193], v[88:91]
	s_nop 7
	s_nop 1
	ds_write_b128 v230, v[194:197] offset:24848
	ds_write_b128 v230, v[198:201] offset:24864
	ds_write_b128 v230, v[202:205] offset:24880
	v_add_u32_e32 v230, 0x6100, v230
	ds_read_b128 v[190:193], v229 offset:13120
	s_waitcnt lgkmcnt(0)
	v_mfma_f32_16x16x32_f16 v[194:197], v[206:209], v[190:193], v[84:87]
	v_mfma_f32_16x16x32_f16 v[198:201], v[210:213], v[190:193], v[76:79]
	v_mfma_f32_16x16x32_f16 v[202:205], v[214:217], v[190:193], v[88:91]
	s_nop 7
	s_nop 1
	ds_write_b128 v230, v[194:197] offset:24848
	ds_write_b128 v230, v[198:201] offset:24864
	ds_write_b128 v230, v[202:205] offset:24880
	ds_write_b128 v231, v[84:87] offset:24848
	ds_write_b128 v231, v[76:79] offset:24864
	ds_write_b128 v231, v[88:91] offset:24880
	ds_read_u16 v232, v176
	ds_read_u16 v177, v176 offset:4160
	s_waitcnt lgkmcnt(0)
	v_mad_u32_u24 v253, v232, s17, v252
	ds_read_b128 v[116:119], v253 offset:24848
	ds_read_b128 v[120:123], v253 offset:24864
	ds_read_b128 v[138:141], v253 offset:24880
	v_mov_b32_e32 v182, 0
	v_mov_b32_e32 v183, 0
	v_mov_b32_e32 v184, 0
	v_mov_b32_e32 v185, 0
	v_mov_b32_e32 v222, 0
	v_mov_b32_e32 v223, 0
	v_mov_b32_e32 v224, 0
	v_mov_b32_e32 v225, 0
	v_mov_b32_e32 v186, 0
	v_mov_b32_e32 v187, 0
	v_mov_b32_e32 v188, 0
	v_mov_b32_e32 v189, 0
	v_mov_b32_e32 v100, 0
	v_mov_b32_e32 v101, 0
	v_mov_b32_e32 v102, 0
	v_mov_b32_e32 v103, 0
	v_mov_b32_e32 v104, 0
	v_mov_b32_e32 v105, 0
	v_mov_b32_e32 v106, 0
	v_mov_b32_e32 v107, 0
	v_mov_b32_e32 v108, 0
	v_mov_b32_e32 v109, 0
	v_mov_b32_e32 v110, 0
	v_mov_b32_e32 v111, 0
	v_mov_b32_e32 v112, 0
	v_mov_b32_e32 v113, 0
	v_mov_b32_e32 v114, 0
	v_mov_b32_e32 v115, 0
	v_mov_b32_e32 v206, 0
	v_mov_b32_e32 v207, 0
	v_mov_b32_e32 v208, 0
	v_mov_b32_e32 v209, 0
	v_mov_b32_e32 v210, 0
	v_mov_b32_e32 v211, 0
	v_mov_b32_e32 v212, 0
	v_mov_b32_e32 v213, 0
	v_mov_b32_e32 v214, 0
	v_mov_b32_e32 v215, 0
	v_mov_b32_e32 v216, 0
	v_mov_b32_e32 v217, 0
	v_mov_b32_e32 v218, 0
	v_mov_b32_e32 v219, 0
	v_mov_b32_e32 v220, 0
	v_mov_b32_e32 v221, 0
	s_waitcnt vmcnt(4) lgkmcnt(0)
	v_readfirstlane_b32 s18, v162
	s_nop 3
	s_cmp_ge_u32 s18, 64
	s_cbranch_scc1 .Lgru_loop_b
.Lgru_loop_a:
	ds_read_b128 v[190:193], v156 offset:0
	ds_read_b128 v[194:197], v156 offset:1024
	ds_read_b128 v[198:201], v156 offset:2048
	ds_read_b128 v[202:205], v156 offset:3072
	s_waitcnt vmcnt(4)
	v_mfma_f32_16x16x32_f16 v[92:95], v[112:115], v[206:209], v[92:95]
	v_exp_f32_e32 v228, v144
	v_exp_f32_e32 v229, v145
	v_exp_f32_e32 v230, v146
	v_exp_f32_e32 v231, v147
	v_exp_f32_e32 v232, v148
	v_exp_f32_e32 v233, v149
	v_exp_f32_e32 v234, v150
	v_exp_f32_e32 v235, v151
	v_mfma_f32_16x16x32_f16 v[92:95], v[108:111], v[210:213], v[92:95]
	v_add_f32_e32 v228, 1.0, v228
	v_add_f32_e32 v229, 1.0, v229
	v_add_f32_e32 v230, 1.0, v230
	v_add_f32_e32 v231, 1.0, v231
	v_add_f32_e32 v232, 1.0, v232
	v_add_f32_e32 v233, 1.0, v233
	v_add_f32_e32 v234, 1.0, v234
	v_add_f32_e32 v235, 1.0, v235
	v_rcp_f32_e32 v228, v228
	v_rcp_f32_e32 v229, v229
	v_rcp_f32_e32 v230, v230
	v_rcp_f32_e32 v231, v231
	v_mfma_f32_16x16x32_f16 v[92:95], v[104:107], v[214:217], v[92:95]
	v_fma_f32 v236, v228, v152, v182
	v_fma_f32 v237, v229, v153, v183
	v_fma_f32 v238, v230, v154, v184
	v_fma_f32 v239, v231, v155, v185
	v_mad_u32_u24 v253, v177, s17, v252
	ds_read_b128 v[222:225], v253 offset:24848
	ds_read_b128 v[186:189], v253 offset:24864
	ds_read_b128 v[182:185], v253 offset:24880
	ds_read_u16 v177, v176 offset:4162
	v_exp_f32_e32 v236, v236
	v_exp_f32_e32 v237, v237
	v_exp_f32_e32 v238, v238
	v_exp_f32_e32 v239, v239
	v_rcp_f32_e32 v232, v232
	v_rcp_f32_e32 v233, v233
	v_mfma_f32_16x16x32_f16 v[92:95], v[100:103], v[218:221], v[92:95]
	global_load_dwordx4 v[112:115], v[166:167], off offset:-2048
	global_load_dwordx4 v[108:111], v[166:167], off offset:-1024
	global_load_dwordx4 v[104:107], v[166:167], off
	global_load_dwordx4 v[100:103], v[166:167], off offset:1024
	v_rcp_f32_e32 v234, v234
	v_rcp_f32_e32 v235, v235
	v_add_f32_e32 v236, 1.0, v236
	v_add_f32_e32 v237, 1.0, v237
	v_add_f32_e32 v238, 1.0, v238
	v_add_f32_e32 v239, 1.0, v239
	v_rcp_f32_e32 v236, v236
	v_rcp_f32_e32 v237, v237
	v_rcp_f32_e32 v238, v238
	v_rcp_f32_e32 v239, v239
	v_pk_fma_f32 v[236:237], v[236:237], -2.0, 1.0 op_sel_hi:[1,0,0]
	v_pk_fma_f32 v[238:239], v[238:239], -2.0, 1.0 op_sel_hi:[1,0,0]
	v_pk_add_f32 v[240:241], v[168:169], v[236:237] neg_lo:[0,1] neg_hi:[0,1]
	v_pk_add_f32 v[242:243], v[170:171], v[238:239] neg_lo:[0,1] neg_hi:[0,1]
	v_pk_fma_f32 v[168:169], v[232:233], v[240:241], v[236:237]
	v_pk_fma_f32 v[170:171], v[234:235], v[242:243], v[238:239]
	v_cvt_pk_f16_f32 v244, v168, v169
	v_cvt_pk_f16_f32 v245, v170, v171
	ds_write_b64 v163, v[244:245] offset:4096
	s_waitcnt lgkmcnt(8)
	v_mfma_f32_16x16x32_f16 v[124:127], v[12:15], v[190:193], v[116:119]
	v_mfma_f32_16x16x32_f16 v[128:131], v[28:31], v[190:193], v[120:123]
	v_mfma_f32_16x16x32_f16 v[132:135], v[32:35], v[190:193], v[80:83]
	s_waitcnt lgkmcnt(7)
	v_mfma_f32_16x16x32_f16 v[124:127], v[16:19], v[194:197], v[124:127]
	v_mfma_f32_16x16x32_f16 v[128:131], v[48:51], v[194:197], v[128:131]
	v_mfma_f32_16x16x32_f16 v[132:135], v[36:39], v[194:197], v[132:135]
	s_waitcnt lgkmcnt(6)
	v_mfma_f32_16x16x32_f16 v[124:127], v[20:23], v[198:201], v[124:127]
	v_mfma_f32_16x16x32_f16 v[128:131], v[52:55], v[198:201], v[128:131]
	v_mfma_f32_16x16x32_f16 v[132:135], v[40:43], v[198:201], v[132:135]
	s_waitcnt lgkmcnt(5)
	v_mfma_f32_16x16x32_f16 v[124:127], v[24:27], v[202:205], v[124:127]
	v_mfma_f32_16x16x32_f16 v[128:131], v[56:59], v[202:205], v[128:131]
	v_mfma_f32_16x16x32_f16 v[132:135], v[44:47], v[202:205], v[132:135]
	s_waitcnt lgkmcnt(0)
	s_barrier
	ds_read_b128 v[206:209], v156 offset:4096
	ds_read_b128 v[210:213], v156 offset:5120
	ds_read_b128 v[214:217], v156 offset:6144
	ds_read_b128 v[218:221], v156 offset:7168
	s_waitcnt vmcnt(4)
	v_mfma_f32_16x16x32_f16 v[96:99], v[72:75], v[190:193], v[96:99]
	v_exp_f32_e32 v228, v124
	v_exp_f32_e32 v229, v125
	v_exp_f32_e32 v230, v126
	v_exp_f32_e32 v231, v127
	v_exp_f32_e32 v232, v128
	v_exp_f32_e32 v233, v129
	v_exp_f32_e32 v234, v130
	v_exp_f32_e32 v235, v131
	v_mfma_f32_16x16x32_f16 v[96:99], v[8:11], v[194:197], v[96:99]
	v_add_f32_e32 v228, 1.0, v228
	v_add_f32_e32 v229, 1.0, v229
	v_add_f32_e32 v230, 1.0, v230
	v_add_f32_e32 v231, 1.0, v231
	v_add_f32_e32 v232, 1.0, v232
	v_add_f32_e32 v233, 1.0, v233
	v_add_f32_e32 v234, 1.0, v234
	v_add_f32_e32 v235, 1.0, v235
	v_rcp_f32_e32 v228, v228
	v_rcp_f32_e32 v229, v229
	v_rcp_f32_e32 v230, v230
	v_rcp_f32_e32 v231, v231
	v_mfma_f32_16x16x32_f16 v[96:99], v[4:7], v[198:201], v[96:99]
	v_fma_f32 v236, v228, v132, v138
	v_fma_f32 v237, v229, v133, v139
	v_fma_f32 v238, v230, v134, v140
	v_fma_f32 v239, v231, v135, v141
	v_mad_u32_u24 v253, v178, s17, v252
	ds_read_b128 v[116:119], v253 offset:24848
	ds_read_b128 v[120:123], v253 offset:24864
	ds_read_b128 v[138:141], v253 offset:24880
	ds_read_u16 v178, v176 offset:4
	v_exp_f32_e32 v236, v236
	v_exp_f32_e32 v237, v237
	v_exp_f32_e32 v238, v238
	v_exp_f32_e32 v239, v239
	v_rcp_f32_e32 v232, v232
	v_rcp_f32_e32 v233, v233
	v_mfma_f32_16x16x32_f16 v[96:99], v[0:3], v[202:205], v[96:99]
	v_rcp_f32_e32 v234, v234
	v_rcp_f32_e32 v235, v235
	v_add_f32_e32 v236, 1.0, v236
	v_add_f32_e32 v237, 1.0, v237
	v_add_f32_e32 v238, 1.0, v238
	v_add_f32_e32 v239, 1.0, v239
	v_rcp_f32_e32 v236, v236
	v_rcp_f32_e32 v237, v237
	v_rcp_f32_e32 v238, v238
	v_rcp_f32_e32 v239, v239
	v_pk_fma_f32 v[236:237], v[236:237], -2.0, 1.0 op_sel_hi:[1,0,0]
	v_pk_fma_f32 v[238:239], v[238:239], -2.0, 1.0 op_sel_hi:[1,0,0]
	v_pk_add_f32 v[240:241], v[172:173], v[236:237] neg_lo:[0,1] neg_hi:[0,1]
	v_pk_add_f32 v[242:243], v[174:175], v[238:239] neg_lo:[0,1] neg_hi:[0,1]
	v_pk_fma_f32 v[172:173], v[232:233], v[240:241], v[236:237]
	v_pk_fma_f32 v[174:175], v[234:235], v[242:243], v[238:239]
	v_cvt_pk_f16_f32 v244, v172, v173
	v_cvt_pk_f16_f32 v245, v174, v175
	ds_write_b64 v163, v[244:245]
	s_waitcnt lgkmcnt(8)
	v_mfma_f32_16x16x32_f16 v[144:147], v[12:15], v[206:209], v[222:225]
	v_mfma_f32_16x16x32_f16 v[148:151], v[28:31], v[206:209], v[186:189]
	v_mfma_f32_16x16x32_f16 v[152:155], v[32:35], v[206:209], v[80:83]
	s_waitcnt lgkmcnt(7)
	v_mfma_f32_16x16x32_f16 v[144:147], v[16:19], v[210:213], v[144:147]
	v_mfma_f32_16x16x32_f16 v[148:151], v[48:51], v[210:213], v[148:151]
	v_mfma_f32_16x16x32_f16 v[152:155], v[36:39], v[210:213], v[152:155]
	s_waitcnt lgkmcnt(6)
	v_mfma_f32_16x16x32_f16 v[144:147], v[20:23], v[214:217], v[144:147]
	v_mfma_f32_16x16x32_f16 v[148:151], v[52:55], v[214:217], v[148:151]
	v_mfma_f32_16x16x32_f16 v[152:155], v[40:43], v[214:217], v[152:155]
	s_waitcnt lgkmcnt(5)
	v_mfma_f32_16x16x32_f16 v[144:147], v[24:27], v[218:221], v[144:147]
	v_mfma_f32_16x16x32_f16 v[148:151], v[56:59], v[218:221], v[148:151]
	v_mfma_f32_16x16x32_f16 v[152:155], v[44:47], v[218:221], v[152:155]
	s_waitcnt lgkmcnt(0)
	s_barrier
	ds_read_b128 v[190:193], v156 offset:0
	ds_read_b128 v[194:197], v156 offset:1024
	ds_read_b128 v[198:201], v156 offset:2048
	ds_read_b128 v[202:205], v156 offset:3072
	v_mfma_f32_16x16x32_f16 v[92:95], v[72:75], v[206:209], v[92:95]
	v_exp_f32_e32 v228, v144
	v_exp_f32_e32 v229, v145
	v_exp_f32_e32 v230, v146
	v_exp_f32_e32 v231, v147
	v_exp_f32_e32 v232, v148
	v_exp_f32_e32 v233, v149
	v_exp_f32_e32 v234, v150
	v_exp_f32_e32 v235, v151
	v_mfma_f32_16x16x32_f16 v[92:95], v[8:11], v[210:213], v[92:95]
	v_add_f32_e32 v228, 1.0, v228
	v_add_f32_e32 v229, 1.0, v229
	v_add_f32_e32 v230, 1.0, v230
	v_add_f32_e32 v231, 1.0, v231
	v_add_f32_e32 v232, 1.0, v232
	v_add_f32_e32 v233, 1.0, v233
	v_add_f32_e32 v234, 1.0, v234
	v_add_f32_e32 v235, 1.0, v235
	v_rcp_f32_e32 v228, v228
	v_rcp_f32_e32 v229, v229
	v_rcp_f32_e32 v230, v230
	v_rcp_f32_e32 v231, v231
	v_mfma_f32_16x16x32_f16 v[92:95], v[4:7], v[214:217], v[92:95]
	v_fma_f32 v236, v228, v152, v182
	v_fma_f32 v237, v229, v153, v183
	v_fma_f32 v238, v230, v154, v184
	v_fma_f32 v239, v231, v155, v185
	v_mad_u32_u24 v253, v177, s17, v252
	ds_read_b128 v[222:225], v253 offset:24848
	ds_read_b128 v[186:189], v253 offset:24864
	ds_read_b128 v[182:185], v253 offset:24880
	ds_read_u16 v177, v176 offset:4164
	v_exp_f32_e32 v236, v236
	v_exp_f32_e32 v237, v237
	v_exp_f32_e32 v238, v238
	v_exp_f32_e32 v239, v239
	v_rcp_f32_e32 v232, v232
	v_rcp_f32_e32 v233, v233
	v_mfma_f32_16x16x32_f16 v[92:95], v[0:3], v[218:221], v[92:95]
	s_ashr_i32 s9, s8, 31
	s_lshl_b64 s[12:13], s[8:9], 15
	v_lshl_add_u64 v[246:247], v[158:159], 0, s[12:13]
	global_load_dwordx4 v[72:75], v[246:247], off
	global_load_dwordx4 v[8:11], v[246:247], off offset:1024
	global_load_dwordx4 v[4:7], v[246:247], off offset:2048
	global_load_dwordx4 v[0:3], v[246:247], off offset:3072
	v_rcp_f32_e32 v234, v234
	v_rcp_f32_e32 v235, v235
	v_add_f32_e32 v236, 1.0, v236
	v_add_f32_e32 v237, 1.0, v237
	v_add_f32_e32 v238, 1.0, v238
	v_add_f32_e32 v239, 1.0, v239
	v_rcp_f32_e32 v236, v236
	v_rcp_f32_e32 v237, v237
	v_rcp_f32_e32 v238, v238
	v_rcp_f32_e32 v239, v239
	v_pk_fma_f32 v[236:237], v[236:237], -2.0, 1.0 op_sel_hi:[1,0,0]
	v_pk_fma_f32 v[238:239], v[238:239], -2.0, 1.0 op_sel_hi:[1,0,0]
	v_pk_add_f32 v[240:241], v[168:169], v[236:237] neg_lo:[0,1] neg_hi:[0,1]
	v_pk_add_f32 v[242:243], v[170:171], v[238:239] neg_lo:[0,1] neg_hi:[0,1]
	v_pk_fma_f32 v[168:169], v[232:233], v[240:241], v[236:237]
	v_pk_fma_f32 v[170:171], v[234:235], v[242:243], v[238:239]
	v_cvt_pk_f16_f32 v244, v168, v169
	v_cvt_pk_f16_f32 v245, v170, v171
	ds_write_b64 v163, v[244:245] offset:4096
	s_waitcnt lgkmcnt(8)
	v_mfma_f32_16x16x32_f16 v[124:127], v[12:15], v[190:193], v[116:119]
	v_mfma_f32_16x16x32_f16 v[128:131], v[28:31], v[190:193], v[120:123]
	v_mfma_f32_16x16x32_f16 v[132:135], v[32:35], v[190:193], v[80:83]
	s_waitcnt lgkmcnt(7)
	v_mfma_f32_16x16x32_f16 v[124:127], v[16:19], v[194:197], v[124:127]
	v_mfma_f32_16x16x32_f16 v[128:131], v[48:51], v[194:197], v[128:131]
	v_mfma_f32_16x16x32_f16 v[132:135], v[36:39], v[194:197], v[132:135]
	s_waitcnt lgkmcnt(6)
	v_mfma_f32_16x16x32_f16 v[124:127], v[20:23], v[198:201], v[124:127]
	v_mfma_f32_16x16x32_f16 v[128:131], v[52:55], v[198:201], v[128:131]
	v_mfma_f32_16x16x32_f16 v[132:135], v[40:43], v[198:201], v[132:135]
	s_waitcnt lgkmcnt(5)
	v_mfma_f32_16x16x32_f16 v[124:127], v[24:27], v[202:205], v[124:127]
	v_mfma_f32_16x16x32_f16 v[128:131], v[56:59], v[202:205], v[128:131]
	v_mfma_f32_16x16x32_f16 v[132:135], v[44:47], v[202:205], v[132:135]
	s_waitcnt lgkmcnt(0)
	s_barrier
	ds_read_b128 v[206:209], v156 offset:4096
	ds_read_b128 v[210:213], v156 offset:5120
	ds_read_b128 v[214:217], v156 offset:6144
	ds_read_b128 v[218:221], v156 offset:7168
	s_waitcnt vmcnt(4)
	v_mfma_f32_16x16x32_f16 v[96:99], v[112:115], v[190:193], v[96:99]
	v_exp_f32_e32 v228, v124
	v_exp_f32_e32 v229, v125
	v_exp_f32_e32 v230, v126
	v_exp_f32_e32 v231, v127
	v_exp_f32_e32 v232, v128
	v_exp_f32_e32 v233, v129
	v_exp_f32_e32 v234, v130
	v_exp_f32_e32 v235, v131
	v_mfma_f32_16x16x32_f16 v[96:99], v[108:111], v[194:197], v[96:99]
	v_add_f32_e32 v228, 1.0, v228
	v_add_f32_e32 v229, 1.0, v229
	v_add_f32_e32 v230, 1.0, v230
	v_add_f32_e32 v231, 1.0, v231
	v_add_f32_e32 v232, 1.0, v232
	v_add_f32_e32 v233, 1.0, v233
	v_add_f32_e32 v234, 1.0, v234
	v_add_f32_e32 v235, 1.0, v235
	v_rcp_f32_e32 v228, v228
	v_rcp_f32_e32 v229, v229
	v_rcp_f32_e32 v230, v230
	v_rcp_f32_e32 v231, v231
	v_mfma_f32_16x16x32_f16 v[96:99], v[104:107], v[198:201], v[96:99]
	v_fma_f32 v236, v228, v132, v138
	v_fma_f32 v237, v229, v133, v139
	v_fma_f32 v238, v230, v134, v140
	v_fma_f32 v239, v231, v135, v141
	v_mad_u32_u24 v253, v178, s17, v252
	ds_read_b128 v[116:119], v253 offset:24848
	ds_read_b128 v[120:123], v253 offset:24864
	ds_read_b128 v[138:141], v253 offset:24880
	ds_read_u16 v178, v176 offset:6
	v_exp_f32_e32 v236, v236
	v_exp_f32_e32 v237, v237
	v_exp_f32_e32 v238, v238
	v_exp_f32_e32 v239, v239
	v_rcp_f32_e32 v232, v232
	v_rcp_f32_e32 v233, v233
	v_mfma_f32_16x16x32_f16 v[96:99], v[100:103], v[202:205], v[96:99]
	v_rcp_f32_e32 v234, v234
	v_rcp_f32_e32 v235, v235
	v_add_f32_e32 v236, 1.0, v236
	v_add_f32_e32 v237, 1.0, v237
	v_add_f32_e32 v238, 1.0, v238
	v_add_f32_e32 v239, 1.0, v239
	v_rcp_f32_e32 v236, v236
	v_rcp_f32_e32 v237, v237
	v_rcp_f32_e32 v238, v238
	v_rcp_f32_e32 v239, v239
	v_pk_fma_f32 v[236:237], v[236:237], -2.0, 1.0 op_sel_hi:[1,0,0]
	v_pk_fma_f32 v[238:239], v[238:239], -2.0, 1.0 op_sel_hi:[1,0,0]
	v_pk_add_f32 v[240:241], v[172:173], v[236:237] neg_lo:[0,1] neg_hi:[0,1]
	v_pk_add_f32 v[242:243], v[174:175], v[238:239] neg_lo:[0,1] neg_hi:[0,1]
	v_pk_fma_f32 v[172:173], v[232:233], v[240:241], v[236:237]
	v_pk_fma_f32 v[174:175], v[234:235], v[242:243], v[238:239]
	v_cvt_pk_f16_f32 v244, v172, v173
	v_cvt_pk_f16_f32 v245, v174, v175
	ds_write_b64 v163, v[244:245]
	s_waitcnt lgkmcnt(8)
	v_mfma_f32_16x16x32_f16 v[144:147], v[12:15], v[206:209], v[222:225]
	v_mfma_f32_16x16x32_f16 v[148:151], v[28:31], v[206:209], v[186:189]
	v_mfma_f32_16x16x32_f16 v[152:155], v[32:35], v[206:209], v[80:83]
	s_waitcnt lgkmcnt(7)
	v_mfma_f32_16x16x32_f16 v[144:147], v[16:19], v[210:213], v[144:147]
	v_mfma_f32_16x16x32_f16 v[148:151], v[48:51], v[210:213], v[148:151]
	v_mfma_f32_16x16x32_f16 v[152:155], v[36:39], v[210:213], v[152:155]
	s_waitcnt lgkmcnt(6)
	v_mfma_f32_16x16x32_f16 v[144:147], v[20:23], v[214:217], v[144:147]
	v_mfma_f32_16x16x32_f16 v[148:151], v[52:55], v[214:217], v[148:151]
	v_mfma_f32_16x16x32_f16 v[152:155], v[40:43], v[214:217], v[152:155]
	s_waitcnt lgkmcnt(5)
	v_mfma_f32_16x16x32_f16 v[144:147], v[24:27], v[218:221], v[144:147]
	v_mfma_f32_16x16x32_f16 v[148:151], v[56:59], v[218:221], v[148:151]
	v_mfma_f32_16x16x32_f16 v[152:155], v[44:47], v[218:221], v[152:155]
	s_add_i32 s5, s5, 2
	s_add_i32 s8, s8, s4
	v_add_u32_e32 v176, 4, v176
	v_lshl_add_u64 v[166:167], v[166:167], 0, s[6:7]
	s_cmpk_gt_u32 s5, 0x7d
	s_waitcnt lgkmcnt(0)
	s_barrier
	s_cbranch_scc0 .Lgru_loop_a
	s_branch .Lgru_tail
.Lgru_loop_b:
.Lgru_loop_b2:
	ds_read_b128 v[190:193], v156 offset:0
	ds_read_b128 v[194:197], v156 offset:1024
	ds_read_b128 v[198:201], v156 offset:2048
	ds_read_b128 v[202:205], v156 offset:3072
	s_waitcnt vmcnt(4)
	v_mfma_f32_16x16x32_f16 v[92:95], v[112:115], v[206:209], v[92:95]
	v_mfma_f32_16x16x32_f16 v[92:95], v[108:111], v[210:213], v[92:95]
	v_mfma_f32_16x16x32_f16 v[92:95], v[104:107], v[214:217], v[92:95]
	v_mfma_f32_16x16x32_f16 v[92:95], v[100:103], v[218:221], v[92:95]
	global_load_dwordx4 v[112:115], v[166:167], off offset:-2048
	global_load_dwordx4 v[108:111], v[166:167], off offset:-1024
	global_load_dwordx4 v[104:107], v[166:167], off
	global_load_dwordx4 v[100:103], v[166:167], off offset:1024
	s_waitcnt lgkmcnt(3)
	v_mfma_f32_16x16x32_f16 v[124:127], v[12:15], v[190:193], v[116:119]
	v_mfma_f32_16x16x32_f16 v[128:131], v[28:31], v[190:193], v[120:123]
	v_mfma_f32_16x16x32_f16 v[132:135], v[32:35], v[190:193], v[80:83]
	s_waitcnt lgkmcnt(2)
	v_mfma_f32_16x16x32_f16 v[124:127], v[16:19], v[194:197], v[124:127]
	v_mfma_f32_16x16x32_f16 v[128:131], v[48:51], v[194:197], v[128:131]
	v_mfma_f32_16x16x32_f16 v[132:135], v[36:39], v[194:197], v[132:135]
	s_waitcnt lgkmcnt(1)
	v_mfma_f32_16x16x32_f16 v[124:127], v[20:23], v[198:201], v[124:127]
	v_mfma_f32_16x16x32_f16 v[128:131], v[52:55], v[198:201], v[128:131]
	v_mfma_f32_16x16x32_f16 v[132:135], v[40:43], v[198:201], v[132:135]
	s_waitcnt lgkmcnt(0)
	v_mfma_f32_16x16x32_f16 v[124:127], v[24:27], v[202:205], v[124:127]
	v_mfma_f32_16x16x32_f16 v[128:131], v[56:59], v[202:205], v[128:131]
	v_exp_f32_e32 v228, v144
	v_exp_f32_e32 v229, v145
	v_exp_f32_e32 v230, v146
	v_exp_f32_e32 v231, v147
	v_exp_f32_e32 v232, v148
	v_exp_f32_e32 v233, v149
	v_exp_f32_e32 v234, v150
	v_exp_f32_e32 v235, v151
	v_add_f32_e32 v228, 1.0, v228
	v_add_f32_e32 v229, 1.0, v229
	v_add_f32_e32 v230, 1.0, v230
	v_add_f32_e32 v231, 1.0, v231
	v_add_f32_e32 v232, 1.0, v232
	v_add_f32_e32 v233, 1.0, v233
	v_add_f32_e32 v234, 1.0, v234
	v_add_f32_e32 v235, 1.0, v235
	v_rcp_f32_e32 v228, v228
	v_rcp_f32_e32 v229, v229
	v_rcp_f32_e32 v230, v230
	v_rcp_f32_e32 v231, v231
	v_fma_f32 v236, v228, v152, v182
	v_fma_f32 v237, v229, v153, v183
	v_fma_f32 v238, v230, v154, v184
	v_fma_f32 v239, v231, v155, v185
	v_mad_u32_u24 v253, v177, s17, v252
	ds_read_b128 v[222:225], v253 offset:24848
	ds_read_b128 v[186:189], v253 offset:24864
	ds_read_b128 v[182:185], v253 offset:24880
	ds_read_u16 v177, v176 offset:4162
	v_exp_f32_e32 v236, v236
	v_exp_f32_e32 v237, v237
	v_exp_f32_e32 v238, v238
	v_exp_f32_e32 v239, v239
	v_rcp_f32_e32 v232, v232
	v_rcp_f32_e32 v233, v233
	v_rcp_f32_e32 v234, v234
	v_rcp_f32_e32 v235, v235
	v_add_f32_e32 v236, 1.0, v236
	v_add_f32_e32 v237, 1.0, v237
	v_add_f32_e32 v238, 1.0, v238
	v_add_f32_e32 v239, 1.0, v239
	v_rcp_f32_e32 v236, v236
	v_rcp_f32_e32 v237, v237
	v_rcp_f32_e32 v238, v238
	v_rcp_f32_e32 v239, v239
	v_pk_fma_f32 v[236:237], v[236:237], -2.0, 1.0 op_sel_hi:[1,0,0]
	v_pk_fma_f32 v[238:239], v[238:239], -2.0, 1.0 op_sel_hi:[1,0,0]
	v_pk_add_f32 v[240:241], v[168:169], v[236:237] neg_lo:[0,1] neg_hi:[0,1]
	v_pk_add_f32 v[242:243], v[170:171], v[238:239] neg_lo:[0,1] neg_hi:[0,1]
	v_pk_fma_f32 v[168:169], v[232:233], v[240:241], v[236:237]
	v_pk_fma_f32 v[170:171], v[234:235], v[242:243], v[238:239]
	v_cvt_pk_f16_f32 v244, v168, v169
	v_cvt_pk_f16_f32 v245, v170, v171
	ds_write_b64 v163, v[244:245] offset:4096
	v_mfma_f32_16x16x32_f16 v[132:135], v[44:47], v[202:205], v[132:135]
	s_waitcnt lgkmcnt(0)
	s_barrier
	ds_read_b128 v[206:209], v156 offset:4096
	ds_read_b128 v[210:213], v156 offset:5120
	ds_read_b128 v[214:217], v156 offset:6144
	ds_read_b128 v[218:221], v156 offset:7168
	s_waitcnt vmcnt(4)
	v_mfma_f32_16x16x32_f16 v[96:99], v[72:75], v[190:193], v[96:99]
	v_mfma_f32_16x16x32_f16 v[96:99], v[8:11], v[194:197], v[96:99]
	v_mfma_f32_16x16x32_f16 v[96:99], v[4:7], v[198:201], v[96:99]
	v_mfma_f32_16x16x32_f16 v[96:99], v[0:3], v[202:205], v[96:99]
	s_waitcnt lgkmcnt(3)
	v_mfma_f32_16x16x32_f16 v[144:147], v[12:15], v[206:209], v[222:225]
	v_mfma_f32_16x16x32_f16 v[148:151], v[28:31], v[206:209], v[186:189]
	v_mfma_f32_16x16x32_f16 v[152:155], v[32:35], v[206:209], v[80:83]
	s_waitcnt lgkmcnt(2)
	v_mfma_f32_16x16x32_f16 v[144:147], v[16:19], v[210:213], v[144:147]
	v_mfma_f32_16x16x32_f16 v[148:151], v[48:51], v[210:213], v[148:151]
	v_mfma_f32_16x16x32_f16 v[152:155], v[36:39], v[210:213], v[152:155]
	s_waitcnt lgkmcnt(1)
	v_mfma_f32_16x16x32_f16 v[144:147], v[20:23], v[214:217], v[144:147]
	v_mfma_f32_16x16x32_f16 v[148:151], v[52:55], v[214:217], v[148:151]
	v_mfma_f32_16x16x32_f16 v[152:155], v[40:43], v[214:217], v[152:155]
	s_waitcnt lgkmcnt(0)
	v_mfma_f32_16x16x32_f16 v[144:147], v[24:27], v[218:221], v[144:147]
	v_mfma_f32_16x16x32_f16 v[148:151], v[56:59], v[218:221], v[148:151]
	v_exp_f32_e32 v228, v124
	v_exp_f32_e32 v229, v125
	v_exp_f32_e32 v230, v126
	v_exp_f32_e32 v231, v127
	v_exp_f32_e32 v232, v128
	v_exp_f32_e32 v233, v129
	v_exp_f32_e32 v234, v130
	v_exp_f32_e32 v235, v131
	v_add_f32_e32 v228, 1.0, v228
	v_add_f32_e32 v229, 1.0, v229
	v_add_f32_e32 v230, 1.0, v230
	v_add_f32_e32 v231, 1.0, v231
	v_add_f32_e32 v232, 1.0, v232
	v_add_f32_e32 v233, 1.0, v233
	v_add_f32_e32 v234, 1.0, v234
	v_add_f32_e32 v235, 1.0, v235
	v_rcp_f32_e32 v228, v228
	v_rcp_f32_e32 v229, v229
	v_rcp_f32_e32 v230, v230
	v_rcp_f32_e32 v231, v231
	v_fma_f32 v236, v228, v132, v138
	v_fma_f32 v237, v229, v133, v139
	v_fma_f32 v238, v230, v134, v140
	v_fma_f32 v239, v231, v135, v141
	v_mad_u32_u24 v253, v178, s17, v252
	ds_read_b128 v[116:119], v253 offset:24848
	ds_read_b128 v[120:123], v253 offset:24864
	ds_read_b128 v[138:141], v253 offset:24880
	ds_read_u16 v178, v176 offset:4
	v_exp_f32_e32 v236, v236
	v_exp_f32_e32 v237, v237
	v_exp_f32_e32 v238, v238
	v_exp_f32_e32 v239, v239
	v_rcp_f32_e32 v232, v232
	v_rcp_f32_e32 v233, v233
	v_rcp_f32_e32 v234, v234
	v_rcp_f32_e32 v235, v235
	v_add_f32_e32 v236, 1.0, v236
	v_add_f32_e32 v237, 1.0, v237
	v_add_f32_e32 v238, 1.0, v238
	v_add_f32_e32 v239, 1.0, v239
	v_rcp_f32_e32 v236, v236
	v_rcp_f32_e32 v237, v237
	v_rcp_f32_e32 v238, v238
	v_rcp_f32_e32 v239, v239
	v_pk_fma_f32 v[236:237], v[236:237], -2.0, 1.0 op_sel_hi:[1,0,0]
	v_pk_fma_f32 v[238:239], v[238:239], -2.0, 1.0 op_sel_hi:[1,0,0]
	v_pk_add_f32 v[240:241], v[172:173], v[236:237] neg_lo:[0,1] neg_hi:[0,1]
	v_pk_add_f32 v[242:243], v[174:175], v[238:239] neg_lo:[0,1] neg_hi:[0,1]
	v_pk_fma_f32 v[172:173], v[232:233], v[240:241], v[236:237]
	v_pk_fma_f32 v[174:175], v[234:235], v[242:243], v[238:239]
	v_cvt_pk_f16_f32 v244, v172, v173
	v_cvt_pk_f16_f32 v245, v174, v175
	ds_write_b64 v163, v[244:245]
	v_mfma_f32_16x16x32_f16 v[152:155], v[44:47], v[218:221], v[152:155]
	s_waitcnt lgkmcnt(0)
	s_barrier
	ds_read_b128 v[190:193], v156 offset:0
	ds_read_b128 v[194:197], v156 offset:1024
	ds_read_b128 v[198:201], v156 offset:2048
	ds_read_b128 v[202:205], v156 offset:3072
	v_mfma_f32_16x16x32_f16 v[92:95], v[72:75], v[206:209], v[92:95]
	v_mfma_f32_16x16x32_f16 v[92:95], v[8:11], v[210:213], v[92:95]
	v_mfma_f32_16x16x32_f16 v[92:95], v[4:7], v[214:217], v[92:95]
	v_mfma_f32_16x16x32_f16 v[92:95], v[0:3], v[218:221], v[92:95]
	s_ashr_i32 s9, s8, 31
	s_lshl_b64 s[12:13], s[8:9], 15
	v_lshl_add_u64 v[246:247], v[158:159], 0, s[12:13]
	global_load_dwordx4 v[72:75], v[246:247], off
	global_load_dwordx4 v[8:11], v[246:247], off offset:1024
	global_load_dwordx4 v[4:7], v[246:247], off offset:2048
	global_load_dwordx4 v[0:3], v[246:247], off offset:3072
	s_waitcnt lgkmcnt(3)
	v_mfma_f32_16x16x32_f16 v[124:127], v[12:15], v[190:193], v[116:119]
	v_mfma_f32_16x16x32_f16 v[128:131], v[28:31], v[190:193], v[120:123]
	v_mfma_f32_16x16x32_f16 v[132:135], v[32:35], v[190:193], v[80:83]
	s_waitcnt lgkmcnt(2)
	v_mfma_f32_16x16x32_f16 v[124:127], v[16:19], v[194:197], v[124:127]
	v_mfma_f32_16x16x32_f16 v[128:131], v[48:51], v[194:197], v[128:131]
	v_mfma_f32_16x16x32_f16 v[132:135], v[36:39], v[194:197], v[132:135]
	s_waitcnt lgkmcnt(1)
	v_mfma_f32_16x16x32_f16 v[124:127], v[20:23], v[198:201], v[124:127]
	v_mfma_f32_16x16x32_f16 v[128:131], v[52:55], v[198:201], v[128:131]
	v_mfma_f32_16x16x32_f16 v[132:135], v[40:43], v[198:201], v[132:135]
	s_waitcnt lgkmcnt(0)
	v_mfma_f32_16x16x32_f16 v[124:127], v[24:27], v[202:205], v[124:127]
	v_mfma_f32_16x16x32_f16 v[128:131], v[56:59], v[202:205], v[128:131]
	v_exp_f32_e32 v228, v144
	v_exp_f32_e32 v229, v145
	v_exp_f32_e32 v230, v146
	v_exp_f32_e32 v231, v147
	v_exp_f32_e32 v232, v148
	v_exp_f32_e32 v233, v149
	v_exp_f32_e32 v234, v150
	v_exp_f32_e32 v235, v151
	v_add_f32_e32 v228, 1.0, v228
	v_add_f32_e32 v229, 1.0, v229
	v_add_f32_e32 v230, 1.0, v230
	v_add_f32_e32 v231, 1.0, v231
	v_add_f32_e32 v232, 1.0, v232
	v_add_f32_e32 v233, 1.0, v233
	v_add_f32_e32 v234, 1.0, v234
	v_add_f32_e32 v235, 1.0, v235
	v_rcp_f32_e32 v228, v228
	v_rcp_f32_e32 v229, v229
	v_rcp_f32_e32 v230, v230
	v_rcp_f32_e32 v231, v231
	v_fma_f32 v236, v228, v152, v182
	v_fma_f32 v237, v229, v153, v183
	v_fma_f32 v238, v230, v154, v184
	v_fma_f32 v239, v231, v155, v185
	v_mad_u32_u24 v253, v177, s17, v252
	ds_read_b128 v[222:225], v253 offset:24848
	ds_read_b128 v[186:189], v253 offset:24864
	ds_read_b128 v[182:185], v253 offset:24880
	ds_read_u16 v177, v176 offset:4164
	v_exp_f32_e32 v236, v236
	v_exp_f32_e32 v237, v237
	v_exp_f32_e32 v238, v238
	v_exp_f32_e32 v239, v239
	v_rcp_f32_e32 v232, v232
	v_rcp_f32_e32 v233, v233
	v_rcp_f32_e32 v234, v234
	v_rcp_f32_e32 v235, v235
	v_add_f32_e32 v236, 1.0, v236
	v_add_f32_e32 v237, 1.0, v237
	v_add_f32_e32 v238, 1.0, v238
	v_add_f32_e32 v239, 1.0, v239
	v_rcp_f32_e32 v236, v236
	v_rcp_f32_e32 v237, v237
	v_rcp_f32_e32 v238, v238
	v_rcp_f32_e32 v239, v239
	v_pk_fma_f32 v[236:237], v[236:237], -2.0, 1.0 op_sel_hi:[1,0,0]
	v_pk_fma_f32 v[238:239], v[238:239], -2.0, 1.0 op_sel_hi:[1,0,0]
	v_pk_add_f32 v[240:241], v[168:169], v[236:237] neg_lo:[0,1] neg_hi:[0,1]
	v_pk_add_f32 v[242:243], v[170:171], v[238:239] neg_lo:[0,1] neg_hi:[0,1]
	v_pk_fma_f32 v[168:169], v[232:233], v[240:241], v[236:237]
	v_pk_fma_f32 v[170:171], v[234:235], v[242:243], v[238:239]
	v_cvt_pk_f16_f32 v244, v168, v169
	v_cvt_pk_f16_f32 v245, v170, v171
	ds_write_b64 v163, v[244:245] offset:4096
	v_mfma_f32_16x16x32_f16 v[132:135], v[44:47], v[202:205], v[132:135]
	s_waitcnt lgkmcnt(0)
	s_barrier
	ds_read_b128 v[206:209], v156 offset:4096
	ds_read_b128 v[210:213], v156 offset:5120
	ds_read_b128 v[214:217], v156 offset:6144
	ds_read_b128 v[218:221], v156 offset:7168
	s_waitcnt vmcnt(4)
	v_mfma_f32_16x16x32_f16 v[96:99], v[112:115], v[190:193], v[96:99]
	v_mfma_f32_16x16x32_f16 v[96:99], v[108:111], v[194:197], v[96:99]
	v_mfma_f32_16x16x32_f16 v[96:99], v[104:107], v[198:201], v[96:99]
	v_mfma_f32_16x16x32_f16 v[96:99], v[100:103], v[202:205], v[96:99]
	s_waitcnt lgkmcnt(3)
	v_mfma_f32_16x16x32_f16 v[144:147], v[12:15], v[206:209], v[222:225]
	v_mfma_f32_16x16x32_f16 v[148:151], v[28:31], v[206:209], v[186:189]
	v_mfma_f32_16x16x32_f16 v[152:155], v[32:35], v[206:209], v[80:83]
	s_waitcnt lgkmcnt(2)
	v_mfma_f32_16x16x32_f16 v[144:147], v[16:19], v[210:213], v[144:147]
	v_mfma_f32_16x16x32_f16 v[148:151], v[48:51], v[210:213], v[148:151]
	v_mfma_f32_16x16x32_f16 v[152:155], v[36:39], v[210:213], v[152:155]
	s_waitcnt lgkmcnt(1)
	v_mfma_f32_16x16x32_f16 v[144:147], v[20:23], v[214:217], v[144:147]
	v_mfma_f32_16x16x32_f16 v[148:151], v[52:55], v[214:217], v[148:151]
	v_mfma_f32_16x16x32_f16 v[152:155], v[40:43], v[214:217], v[152:155]
	s_waitcnt lgkmcnt(0)
	v_mfma_f32_16x16x32_f16 v[144:147], v[24:27], v[218:221], v[144:147]
	v_mfma_f32_16x16x32_f16 v[148:151], v[56:59], v[218:221], v[148:151]
	v_exp_f32_e32 v228, v124
	v_exp_f32_e32 v229, v125
	v_exp_f32_e32 v230, v126
	v_exp_f32_e32 v231, v127
	v_exp_f32_e32 v232, v128
	v_exp_f32_e32 v233, v129
	v_exp_f32_e32 v234, v130
	v_exp_f32_e32 v235, v131
	v_add_f32_e32 v228, 1.0, v228
	v_add_f32_e32 v229, 1.0, v229
	v_add_f32_e32 v230, 1.0, v230
	v_add_f32_e32 v231, 1.0, v231
	v_add_f32_e32 v232, 1.0, v232
	v_add_f32_e32 v233, 1.0, v233
	v_add_f32_e32 v234, 1.0, v234
	v_add_f32_e32 v235, 1.0, v235
	v_rcp_f32_e32 v228, v228
	v_rcp_f32_e32 v229, v229
	v_rcp_f32_e32 v230, v230
	v_rcp_f32_e32 v231, v231
	v_fma_f32 v236, v228, v132, v138
	v_fma_f32 v237, v229, v133, v139
	v_fma_f32 v238, v230, v134, v140
	v_fma_f32 v239, v231, v135, v141
	v_mad_u32_u24 v253, v178, s17, v252
	ds_read_b128 v[116:119], v253 offset:24848
	ds_read_b128 v[120:123], v253 offset:24864
	ds_read_b128 v[138:141], v253 offset:24880
	ds_read_u16 v178, v176 offset:6
	v_exp_f32_e32 v236, v236
	v_exp_f32_e32 v237, v237
	v_exp_f32_e32 v238, v238
	v_exp_f32_e32 v239, v239
	v_rcp_f32_e32 v232, v232
	v_rcp_f32_e32 v233, v233
	v_rcp_f32_e32 v234, v234
	v_rcp_f32_e32 v235, v235
	v_add_f32_e32 v236, 1.0, v236
	v_add_f32_e32 v237, 1.0, v237
	v_add_f32_e32 v238, 1.0, v238
	v_add_f32_e32 v239, 1.0, v239
	v_rcp_f32_e32 v236, v236
	v_rcp_f32_e32 v237, v237
	v_rcp_f32_e32 v238, v238
	v_rcp_f32_e32 v239, v239
	v_pk_fma_f32 v[236:237], v[236:237], -2.0, 1.0 op_sel_hi:[1,0,0]
	v_pk_fma_f32 v[238:239], v[238:239], -2.0, 1.0 op_sel_hi:[1,0,0]
	v_pk_add_f32 v[240:241], v[172:173], v[236:237] neg_lo:[0,1] neg_hi:[0,1]
	v_pk_add_f32 v[242:243], v[174:175], v[238:239] neg_lo:[0,1] neg_hi:[0,1]
	v_pk_fma_f32 v[172:173], v[232:233], v[240:241], v[236:237]
	v_pk_fma_f32 v[174:175], v[234:235], v[242:243], v[238:239]
	v_cvt_pk_f16_f32 v244, v172, v173
	v_cvt_pk_f16_f32 v245, v174, v175
	ds_write_b64 v163, v[244:245]
	v_mfma_f32_16x16x32_f16 v[152:155], v[44:47], v[218:221], v[152:155]
	s_add_i32 s5, s5, 2
	s_add_i32 s8, s8, s4
	v_add_u32_e32 v176, 4, v176
	v_lshl_add_u64 v[166:167], v[166:167], 0, s[6:7]
	s_cmpk_gt_u32 s5, 0x7d
	s_waitcnt lgkmcnt(0)
	s_barrier
	s_cbranch_scc0 .Lgru_loop_b2
.Lgru_tail:
	s_waitcnt vmcnt(0)
	v_mfma_f32_16x16x32_f16 v[92:95], v[112:115], v[206:209], v[92:95]
	v_mfma_f32_16x16x32_f16 v[92:95], v[108:111], v[210:213], v[92:95]
	v_mfma_f32_16x16x32_f16 v[92:95], v[104:107], v[214:217], v[92:95]
	v_mfma_f32_16x16x32_f16 v[92:95], v[100:103], v[218:221], v[92:95]
	ds_read_b128 v[190:193], v156 offset:0
	ds_read_b128 v[194:197], v156 offset:1024
	ds_read_b128 v[198:201], v156 offset:2048
	ds_read_b128 v[202:205], v156 offset:3072
	v_exp_f32_e32 v228, v144
	v_exp_f32_e32 v229, v145
	v_exp_f32_e32 v230, v146
	v_exp_f32_e32 v231, v147
	v_exp_f32_e32 v232, v148
	v_exp_f32_e32 v233, v149
	v_exp_f32_e32 v234, v150
	v_exp_f32_e32 v235, v151
	v_add_f32_e32 v228, 1.0, v228
	v_add_f32_e32 v229, 1.0, v229
	v_add_f32_e32 v230, 1.0, v230
	v_add_f32_e32 v231, 1.0, v231
	v_add_f32_e32 v232, 1.0, v232
	v_add_f32_e32 v233, 1.0, v233
	v_add_f32_e32 v234, 1.0, v234
	v_add_f32_e32 v235, 1.0, v235
	v_rcp_f32_e32 v228, v228
	v_rcp_f32_e32 v229, v229
	v_rcp_f32_e32 v230, v230
	v_rcp_f32_e32 v231, v231
	v_fma_f32 v236, v228, v152, v182
	v_fma_f32 v237, v229, v153, v183
	v_fma_f32 v238, v230, v154, v184
	v_fma_f32 v239, v231, v155, v185
	v_exp_f32_e32 v236, v236
	v_exp_f32_e32 v237, v237
	v_exp_f32_e32 v238, v238
	v_exp_f32_e32 v239, v239
	v_rcp_f32_e32 v232, v232
	v_rcp_f32_e32 v233, v233
	v_rcp_f32_e32 v234, v234
	v_rcp_f32_e32 v235, v235
	v_add_f32_e32 v236, 1.0, v236
	v_add_f32_e32 v237, 1.0, v237
	v_add_f32_e32 v238, 1.0, v238
	v_add_f32_e32 v239, 1.0, v239
	v_rcp_f32_e32 v236, v236
	v_rcp_f32_e32 v237, v237
	v_rcp_f32_e32 v238, v238
	v_rcp_f32_e32 v239, v239
	v_pk_fma_f32 v[236:237], v[236:237], -2.0, 1.0 op_sel_hi:[1,0,0]
	v_pk_fma_f32 v[238:239], v[238:239], -2.0, 1.0 op_sel_hi:[1,0,0]
	v_pk_add_f32 v[240:241], v[168:169], v[236:237] neg_lo:[0,1] neg_hi:[0,1]
	v_pk_add_f32 v[242:243], v[170:171], v[238:239] neg_lo:[0,1] neg_hi:[0,1]
	v_pk_fma_f32 v[168:169], v[232:233], v[240:241], v[236:237]
	v_pk_fma_f32 v[170:171], v[234:235], v[242:243], v[238:239]
	v_cvt_pk_f16_f32 v244, v168, v169
	v_cvt_pk_f16_f32 v245, v170, v171
	ds_write_b64 v163, v[244:245] offset:4096
	s_waitcnt lgkmcnt(1)
	v_mfma_f32_16x16x32_f16 v[96:99], v[72:75], v[190:193], v[96:99]
	v_mfma_f32_16x16x32_f16 v[96:99], v[8:11], v[194:197], v[96:99]
	v_mfma_f32_16x16x32_f16 v[96:99], v[4:7], v[198:201], v[96:99]
	v_mfma_f32_16x16x32_f16 v[96:99], v[0:3], v[202:205], v[96:99]
	s_waitcnt lgkmcnt(0)
	s_barrier
	ds_read_b128 v[206:209], v156 offset:4096
	ds_read_b128 v[210:213], v156 offset:5120
	ds_read_b128 v[214:217], v156 offset:6144
	ds_read_b128 v[218:221], v156 offset:7168
	s_lshl_b32 s0, s16, 21
	s_add_u32 s4, s10, s0
	s_addc_u32 s5, s11, 0
	s_lshl_b64 s[0:1], s[2:3], 9
	s_add_u32 s0, s4, s0
	s_addc_u32 s1, s5, s1
	v_lshlrev_b32_e32 v222, 9, v161
	v_mov_b32_e32 v223, 0
	v_lshlrev_b32_e32 v224, 2, v162
	v_mov_b32_e32 v225, 0
	v_lshl_add_u64 v[186:187], s[0:1], 0, v[224:225]
	v_lshlrev_b32_e32 v224, 2, v160
	v_lshl_add_u64 v[186:187], v[186:187], 0, v[224:225]
	v_lshl_add_u64 v[188:189], v[186:187], 0, v[222:223]
	v_or_b32_e32 v222, 0x2000, v222
	v_lshl_add_u64 v[246:247], v[186:187], 0, v[222:223]
	s_waitcnt lgkmcnt(0)
	v_mfma_f32_16x16x32_f16 v[92:95], v[72:75], v[206:209], v[92:95]
	v_mfma_f32_16x16x32_f16 v[92:95], v[8:11], v[210:213], v[92:95]
	v_mfma_f32_16x16x32_f16 v[92:95], v[4:7], v[214:217], v[92:95]
	v_mfma_f32_16x16x32_f16 v[92:95], v[0:3], v[218:221], v[92:95]
	s_nop 7
	s_nop 3
	global_store_dwordx4 v[188:189], v[96:99], off
	global_store_dwordx4 v[246:247], v[92:95], off
	s_endpgm
